# dilated-attention step: xor-16/32 row reductions by permlane swaps instead of ds_bpermute
# speedup vs baseline: 1.0011x; 1.0011x over previous
.LBB0_453:
	v_add_u32_e32 v190, 0, v47
	ds_read_b128 v[156:159], v190
	ds_read_b128 v[160:163], v190 offset:4352
	ds_read_b128 v[182:185], v190 offset:64
	ds_read_b128 v[186:189], v190 offset:4416
	v_mov_b32_e32 v180, v164
	v_cmp_le_i32_e64 s[36:37], s69, v229
	s_waitcnt vmcnt(7) lgkmcnt(3)
	v_mfma_f32_16x16x32_bf16 v[164:167], v[156:159], v[72:75], 0
	v_mov_b32_e32 v181, v231
	v_add_u32_e32 v47, 0x2200, v47
	s_waitcnt lgkmcnt(2)
	v_mfma_f32_16x16x32_bf16 v[168:171], v[160:163], v[72:75], 0
	s_waitcnt vmcnt(3)
	v_mfma_f32_16x16x32_bf16 v[156:159], v[156:159], v[84:87], 0
	v_mfma_f32_16x16x32_bf16 v[160:163], v[160:163], v[84:87], 0
	s_waitcnt lgkmcnt(1)
	v_mfma_f32_16x16x32_bf16 v[164:167], v[182:185], v[68:71], v[164:167]
	s_waitcnt lgkmcnt(0)
	v_mfma_f32_16x16x32_bf16 v[168:171], v[186:189], v[68:71], v[168:171]
	s_waitcnt vmcnt(2)
	v_mfma_f32_16x16x32_bf16 v[156:159], v[182:185], v[80:83], v[156:159]
	v_mfma_f32_16x16x32_bf16 v[160:163], v[186:189], v[80:83], v[160:163]
	ds_read_b128 v[182:185], v190 offset:128
	ds_read_b128 v[186:189], v190 offset:4480
	s_waitcnt lgkmcnt(0)
	v_mfma_f32_16x16x32_bf16 v[232:235], v[186:189], v[64:67], v[168:171]
	s_waitcnt vmcnt(1)
	v_mfma_f32_16x16x32_bf16 v[160:163], v[186:189], v[76:79], v[160:163]
	ds_read_b128 v[186:189], v190 offset:192
	ds_read_b128 v[236:239], v190 offset:4544
	v_mfma_f32_16x16x32_bf16 v[164:167], v[182:185], v[64:67], v[164:167]
	v_mfma_f32_16x16x32_bf16 v[182:185], v[182:185], v[76:79], v[156:159]
	s_waitcnt lgkmcnt(0)
	v_mfma_f32_16x16x32_bf16 v[156:159], v[236:239], v[60:63], v[232:235]
	v_mfma_f32_16x16x32_bf16 v[168:171], v[186:189], v[60:63], v[164:167]
	s_waitcnt vmcnt(0)
	v_mfma_f32_16x16x32_bf16 v[164:167], v[186:189], v[88:91], v[182:185]
	s_nop 4
	v_mul_f32_e32 v156, 0x3e0293ee, v156
	v_mul_f32_e32 v168, 0x3e0293ee, v168
	v_mul_f32_e32 v169, 0x3e0293ee, v169
	v_subrev_u32_e32 v182, 19, v229
	v_add_u32_e32 v184, s70, v217
	v_add_u32_e32 v183, -3, v229
	v_cmp_le_i32_e32 vcc, s69, v182
	v_add_u32_e32 v182, 0x70, v184
	v_add_u32_e32 v185, 0x80, v184
	v_cmp_gt_u32_e64 s[24:25], s44, v182
	v_cmp_le_i32_e64 s[22:23], s69, v183
	v_cmp_gt_u32_e64 s[0:1], s44, v185
	s_and_b64 s[24:25], s[24:25], s[22:23]
	v_subrev_u32_e32 v183, 18, v229
	s_and_b64 s[0:1], s[0:1], vcc
	v_cndmask_b32_e64 v156, v226, v156, s[24:25]
	v_add_u32_e32 v185, -2, v229
	v_add_u32_e32 v186, 0x7f, v184
	v_cmp_le_i32_e64 s[24:25], s69, v183
	v_add_u32_e32 v183, 0x6f, v184
	v_cndmask_b32_e64 v168, v226, v168, s[0:1]
	v_cmp_gt_u32_e64 s[0:1], s44, v186
	v_cmp_gt_u32_e64 s[28:29], s44, v183
	v_cmp_le_i32_e64 s[26:27], s69, v185
	s_and_b64 s[0:1], s[0:1], s[24:25]
	s_and_b64 s[28:29], s[28:29], s[26:27]
	v_mul_f32_e32 v157, 0x3e0293ee, v157
	v_cndmask_b32_e64 v183, v226, v169, s[0:1]
	v_cndmask_b32_e64 v157, v226, v157, s[28:29]
	v_max_f32_e32 v182, v168, v156
	v_max_f32_e32 v169, v183, v157
	v_max3_f32 v169, v182, s45, v169
	v_subrev_u32_e32 v182, 17, v229
	v_add_u32_e32 v185, -1, v229
	v_add_u32_e32 v186, 0x7e, v184
	v_cmp_le_i32_e64 s[28:29], s69, v182
	v_add_u32_e32 v182, 0x6e, v184
	v_cmp_gt_u32_e64 s[0:1], s44, v186
	v_cmp_gt_u32_e64 s[34:35], s44, v182
	v_cmp_le_i32_e64 s[30:31], s69, v185
	s_and_b64 s[0:1], s[0:1], s[28:29]
	s_and_b64 s[34:35], s[34:35], s[30:31]
	v_mul_f32_e32 v170, 0x3e0293ee, v170
	v_mul_f32_e32 v158, 0x3e0293ee, v158
	v_add_u32_e32 v185, -16, v229
	v_add_u32_e32 v186, 0x7d, v184
	v_add_u32_e32 v184, 0x6d, v184
	v_cndmask_b32_e64 v170, v226, v170, s[0:1]
	v_cndmask_b32_e64 v158, v226, v158, s[34:35]
	v_cmp_gt_u32_e64 s[0:1], s44, v186
	v_cmp_le_i32_e64 s[34:35], s69, v185
	v_cmp_gt_u32_e64 s[40:41], s44, v184
	s_and_b64 s[0:1], s[0:1], s[34:35]
	s_and_b64 s[40:41], s[40:41], s[36:37]
	v_mul_f32_e32 v171, 0x3e0293ee, v171
	v_mul_f32_e32 v159, 0x3e0293ee, v159
	v_cndmask_b32_e64 v184, v226, v171, s[0:1]
	v_cndmask_b32_e64 v159, v226, v159, s[40:41]
	v_max_f32_e32 v182, v170, v158
	v_max_f32_e32 v171, v184, v159
	v_max3_f32 v169, v169, v182, v171
	v_mov_b32_e32 v171, v169
	s_nop 1
	v_permlane16_swap_b32_e32 v169, v171
	v_mfma_f32_16x16x32_bf16 v[160:163], v[236:239], v[88:91], v[160:163]
	v_mul_f32_e32 v164, 0x3e0293ee, v164
	v_mul_f32_e32 v165, 0x3e0293ee, v165
	v_mul_f32_e32 v166, 0x3e0293ee, v166
	s_waitcnt lgkmcnt(0)
	v_max_f32_e32 v171, v171, v171
	v_max_f32_e32 v169, v169, v171
	v_mov_b32_e32 v171, v169
	s_nop 1
	v_permlane32_swap_b32_e32 v169, v171
	s_nop 0
	v_mul_f32_e32 v160, 0x3e0293ee, v160
	v_mul_f32_e32 v161, 0x3e0293ee, v161
	v_mul_f32_e32 v162, 0x3e0293ee, v162
	v_mul_f32_e32 v167, 0x3e0293ee, v167
	s_waitcnt lgkmcnt(0)
	v_max3_f32 v231, v181, v169, v171
	v_sub_f32_e32 v156, v156, v231
	v_sub_f32_e32 v168, v168, v231
	v_exp_f32_e32 v169, v156
	v_sub_f32_e32 v156, v183, v231
	v_exp_f32_e32 v171, v168
	v_exp_f32_e32 v183, v156
	v_sub_f32_e32 v156, v157, v231
	v_add_u32_e32 v168, s70, v215
	v_sub_f32_e32 v182, v181, v231
	v_exp_f32_e32 v181, v156
	v_sub_f32_e32 v156, v170, v231
	v_add_u32_e32 v170, 0x80, v168
	v_cmp_gt_u32_e64 s[0:1], s44, v170
	v_add_u32_e32 v170, 0x70, v168
	v_exp_f32_e32 v192, v182
	s_and_b64 vcc, s[0:1], vcc
	v_cmp_gt_u32_e64 s[0:1], s44, v170
	v_add_u32_e32 v182, 0x7f, v168
	s_and_b64 s[0:1], s[0:1], s[22:23]
	v_cndmask_b32_e32 v170, v226, v164, vcc
	v_cmp_gt_u32_e32 vcc, s44, v182
	v_add_u32_e32 v182, 0x6f, v168
	v_cndmask_b32_e64 v160, v226, v160, s[0:1]
	v_cmp_gt_u32_e64 s[0:1], s44, v182
	s_and_b64 vcc, vcc, s[24:25]
	s_and_b64 s[0:1], s[0:1], s[26:27]
	v_cndmask_b32_e32 v165, v226, v165, vcc
	v_cndmask_b32_e64 v161, v226, v161, s[0:1]
	v_max_f32_e32 v164, v170, v160
	v_max_f32_e32 v182, v165, v161
	v_max3_f32 v164, v164, s45, v182
	v_add_u32_e32 v182, 0x7e, v168
	v_cmp_gt_u32_e32 vcc, s44, v182
	v_add_u32_e32 v182, 0x6e, v168
	v_exp_f32_e32 v187, v156
	v_sub_f32_e32 v156, v158, v231
	v_cmp_gt_u32_e64 s[0:1], s44, v182
	v_exp_f32_e32 v185, v156
	v_sub_f32_e32 v156, v184, v231
	s_and_b64 vcc, vcc, s[28:29]
	s_and_b64 s[0:1], s[0:1], s[30:31]
	v_add_u32_e32 v184, 0x7d, v168
	v_add_u32_e32 v168, 0x6d, v168
	v_cndmask_b32_e32 v166, v226, v166, vcc
	v_cndmask_b32_e64 v162, v226, v162, s[0:1]
	v_cmp_gt_u32_e32 vcc, s44, v184
	v_cmp_gt_u32_e64 s[0:1], s44, v168
	s_and_b64 vcc, vcc, s[34:35]
	s_and_b64 s[0:1], s[0:1], s[36:37]
	v_mul_f32_e32 v163, 0x3e0293ee, v163
	v_cndmask_b32_e32 v167, v226, v167, vcc
	v_cndmask_b32_e64 v163, v226, v163, s[0:1]
	v_max_f32_e32 v182, v166, v162
	v_max_f32_e32 v168, v167, v163
	v_max3_f32 v164, v164, v182, v168
	v_mov_b32_e32 v168, v164
	s_nop 1
	v_permlane16_swap_b32_e32 v164, v168
	v_exp_f32_e32 v191, v156
	v_sub_f32_e32 v156, v159, v231
	v_exp_f32_e32 v189, v156
	v_cvt_pk_bf16_f32 v156, v171, v183
	s_waitcnt lgkmcnt(0)
	v_max_f32_e32 v168, v168, v168
	v_max_f32_e32 v164, v164, v168
	v_mov_b32_e32 v168, v164
	s_nop 1
	v_permlane32_swap_b32_e32 v164, v168
	v_cvt_pk_bf16_f32 v157, v187, v191
	v_cvt_pk_bf16_f32 v158, v169, v181
	v_cvt_pk_bf16_f32 v159, v185, v189
	v_pk_mul_f32 v[154:155], v[154:155], v[192:193] op_sel_hi:[1,0]
	s_waitcnt lgkmcnt(0)
	v_max3_f32 v164, v180, v164, v168
	v_sub_f32_e32 v168, v170, v164
	v_sub_f32_e32 v160, v160, v164
	v_exp_f32_e32 v170, v168
	v_exp_f32_e32 v168, v160
	v_sub_f32_e32 v160, v165, v164
	v_exp_f32_e32 v182, v160
	v_sub_f32_e32 v160, v161, v164
	v_sub_f32_e32 v232, v180, v164
	v_exp_f32_e32 v180, v160
	v_sub_f32_e32 v160, v166, v164
	v_exp_f32_e32 v186, v160
	v_sub_f32_e32 v160, v162, v164
	v_exp_f32_e32 v184, v160
	v_sub_f32_e32 v160, v167, v164
	v_exp_f32_e32 v190, v160
	v_sub_f32_e32 v160, v163, v164
	v_exp_f32_e32 v188, v160
	v_pk_add_f32 v[162:163], v[170:171], v[168:169]
	v_pk_add_f32 v[166:167], v[182:183], v[180:181]
	v_pk_add_f32 v[162:163], v[162:163], 0 op_sel_hi:[1,0]
	v_exp_f32_e32 v160, v232
	v_pk_add_f32 v[162:163], v[166:167], v[162:163]
	v_pk_add_f32 v[166:167], v[186:187], v[184:185]
	v_add_u32_e32 v165, 0, v230
	v_pk_add_f32 v[162:163], v[166:167], v[162:163]
	v_pk_add_f32 v[166:167], v[190:191], v[188:189]
	v_mov_b32_e32 v161, v192
	v_pk_add_f32 v[162:163], v[166:167], v[162:163]
	v_mov_b32_e32 v167, v163
	v_mov_b32_e32 v166, v162
	s_nop 1
	v_permlane16_swap_b32_e32 v163, v167
	v_permlane16_swap_b32_e32 v162, v166
	v_pk_mul_f32 v[122:123], v[122:123], v[160:161] op_sel_hi:[1,0]
	v_pk_mul_f32 v[120:121], v[120:121], v[160:161] op_sel_hi:[1,0]
	v_pk_mul_f32 v[118:119], v[118:119], v[160:161] op_sel_hi:[1,0]
	v_pk_mul_f32 v[116:117], v[116:117], v[160:161] op_sel_hi:[1,0]
	s_waitcnt lgkmcnt(0)
	v_pk_add_f32 v[162:163], v[162:163], v[166:167]
	v_mov_b32_e32 v167, v163
	v_mov_b32_e32 v166, v162
	s_nop 1
	v_permlane32_swap_b32_e32 v163, v167
	v_permlane32_swap_b32_e32 v162, v166
	v_pk_mul_f32 v[114:115], v[114:115], v[160:161] op_sel_hi:[1,0]
	v_pk_mul_f32 v[112:113], v[112:113], v[160:161] op_sel_hi:[1,0]
	v_pk_mul_f32 v[110:111], v[110:111], v[160:161] op_sel_hi:[1,0]
	v_pk_mul_f32 v[108:109], v[108:109], v[160:161] op_sel_hi:[1,0]
	s_waitcnt lgkmcnt(0)
	v_pk_add_f32 v[162:163], v[162:163], v[166:167]
	v_add_u32_e32 v166, 0x10000, v165
	v_pk_fma_f32 v[178:179], v[178:179], v[160:161], v[162:163]
	v_pk_mul_f32 v[102:103], v[102:103], v[160:161] op_sel_hi:[1,0]
	v_pk_mul_f32 v[100:101], v[100:101], v[160:161] op_sel_hi:[1,0]
	v_pk_mul_f32 v[98:99], v[98:99], v[160:161] op_sel_hi:[1,0]
	v_pk_mul_f32 v[96:97], v[96:97], v[160:161] op_sel_hi:[1,0]
	v_pk_mul_f32 v[94:95], v[94:95], v[160:161] op_sel_hi:[1,0]
	v_pk_mul_f32 v[92:93], v[92:93], v[160:161] op_sel_hi:[1,0]
	v_pk_mul_f32 v[106:107], v[106:107], v[160:161] op_sel_hi:[1,0]
	v_pk_mul_f32 v[104:105], v[104:105], v[160:161] op_sel_hi:[1,0]
	v_cvt_pk_bf16_f32 v160, v170, v182
	v_cvt_pk_bf16_f32 v161, v186, v190
	v_cvt_pk_bf16_f32 v162, v168, v180
	v_cvt_pk_bf16_f32 v163, v184, v188
	ds_read_b64_tr_b16 v[168:169], v166
	ds_read_b64_tr_b16 v[166:167], v165 offset:60928
	ds_read_b64_tr_b16 v[180:181], v165 offset:60960
	v_pk_mul_f32 v[152:153], v[152:153], v[192:193] op_sel_hi:[1,0]
	s_waitcnt lgkmcnt(1)
	v_mfma_f32_16x16x32_bf16 v[120:123], v[166:169], v[160:163], v[120:123]
	v_mul_f32_e64 v146, v146, v192
	v_mul_f32_e64 v147, v147, v192
	v_pk_mul_f32 v[144:145], v[144:145], v[192:193] op_sel_hi:[1,0]
	v_pk_mul_f32 v[142:143], v[142:143], v[192:193] op_sel_hi:[1,0]
	v_mfma_f32_16x16x32_bf16 v[152:155], v[166:169], v[156:159], v[152:155]
	v_add_u32_e32 v166, 0x10020, v165
	v_add_u32_e32 v168, 0x10040, v165
	ds_read_b64_tr_b16 v[182:183], v166
	ds_read_b64_tr_b16 v[166:167], v165 offset:60992
	ds_read_b64_tr_b16 v[168:169], v168
	s_waitcnt lgkmcnt(0)
	v_mfma_f32_16x16x32_bf16 v[144:147], v[166:169], v[156:159], v[144:147]
	v_mul_f32_e64 v140, v140, v192
	v_mul_f32_e64 v141, v141, v192
	v_pk_mul_f32 v[134:135], v[134:135], v[192:193] op_sel_hi:[1,0]
	v_pk_mul_f32 v[132:133], v[132:133], v[192:193] op_sel_hi:[1,0]
	v_mfma_f32_16x16x32_bf16 v[112:115], v[166:169], v[160:163], v[112:115]
	v_add_u32_e32 v168, 0x10060, v165
	ds_read_b64_tr_b16 v[166:167], v165 offset:61024
	ds_read_b64_tr_b16 v[168:169], v168
	s_waitcnt lgkmcnt(0)
	v_mfma_f32_16x16x32_bf16 v[140:143], v[166:169], v[156:159], v[140:143]
	v_mul_f32_e64 v130, v130, v192
	v_mul_f32_e64 v131, v131, v192
	v_pk_mul_f32 v[128:129], v[128:129], v[192:193] op_sel_hi:[1,0]
	v_pk_mul_f32 v[126:127], v[126:127], v[192:193] op_sel_hi:[1,0]
	v_mfma_f32_16x16x32_bf16 v[108:111], v[166:169], v[160:163], v[108:111]
	v_add_u32_e32 v168, 0x10080, v165
	ds_read_b64_tr_b16 v[166:167], v165 offset:61056
	ds_read_b64_tr_b16 v[168:169], v168
	s_waitcnt lgkmcnt(0)
	v_mfma_f32_16x16x32_bf16 v[132:135], v[166:169], v[156:159], v[132:135]
	v_mul_f32_e64 v124, v124, v192
	v_mul_f32_e64 v125, v125, v192
	v_pk_mul_f32 v[150:151], v[150:151], v[192:193] op_sel_hi:[1,0]
	v_pk_mul_f32 v[148:149], v[148:149], v[192:193] op_sel_hi:[1,0]
	v_mfma_f32_16x16x32_bf16 v[100:103], v[166:169], v[160:163], v[100:103]
	v_add_u32_e32 v168, 0x100a0, v165
	ds_read_b64_tr_b16 v[166:167], v165 offset:61088
	ds_read_b64_tr_b16 v[168:169], v168
	s_waitcnt lgkmcnt(0)
	v_mfma_f32_16x16x32_bf16 v[128:131], v[166:169], v[156:159], v[128:131]
	v_mul_f32_e64 v138, v138, v192
	v_mul_f32_e64 v139, v139, v192
	v_pk_mul_f32 v[136:137], v[136:137], v[192:193] op_sel_hi:[1,0]
	s_sub_i32 s70, s70, 32
	v_mfma_f32_16x16x32_bf16 v[96:99], v[166:169], v[160:163], v[96:99]
	v_add_u32_e32 v168, 0x100c0, v165
	ds_read_b64_tr_b16 v[166:167], v165 offset:61120
	ds_read_b64_tr_b16 v[168:169], v168
	s_waitcnt lgkmcnt(0)
	v_mfma_f32_16x16x32_bf16 v[124:127], v[166:169], v[156:159], v[124:127]
	v_add_u32_e32 v230, 0x2400, v230
	v_add_u32_e32 v229, 32, v229
	s_cmpk_eq_i32 s70, 0xff60
	v_mfma_f32_16x16x32_bf16 v[92:95], v[166:169], v[160:163], v[92:95]
	ds_read_b64_tr_b16 v[166:167], v165 offset:61152
	v_add_u32_e32 v165, 0x100e0, v165
	ds_read_b64_tr_b16 v[168:169], v165
	v_mfma_f32_16x16x32_bf16 v[148:151], v[180:183], v[156:159], v[148:151]
	v_mfma_f32_16x16x32_bf16 v[116:119], v[180:183], v[160:163], v[116:119]
	s_waitcnt lgkmcnt(0)
	v_mfma_f32_16x16x32_bf16 v[136:139], v[166:169], v[156:159], v[136:139]
	v_mfma_f32_16x16x32_bf16 v[104:107], v[166:169], v[160:163], v[104:107]
	s_cbranch_scc0 .LBB0_453
	s_ashr_i32 s91, s90, 31
	s_add_i32 s68, s68, s33
	s_lshl_b64 s[0:1], s[88:89], 12
	s_lshl_b64 s[22:23], s[90:91], 13
	s_add_u32 s0, s0, s38
	s_addc_u32 s1, s1, 0
	s_add_u32 s0, s0, s22
	s_addc_u32 s1, s1, s23
	v_div_scale_f32 v47, s[22:23], v179, v179, 1.0
	v_rcp_f32_e32 v64, v47
	v_or_b32_e32 v62, s68, v200
	v_mul_lo_u32 v62, v62, s57
	v_mov_b32_e32 v63, v46
	v_fma_f32 v65, -v47, v64, 1.0
	v_fmac_f32_e32 v64, v65, v64
	v_div_scale_f32 v65, vcc, 1.0, v179, 1.0
	v_mul_f32_e32 v66, v65, v64
	v_fma_f32 v67, -v47, v66, v65
	v_fmac_f32_e32 v66, v67, v64
	v_fma_f32 v47, -v47, v66, v65
	v_lshl_add_u64 v[62:63], s[0:1], 0, v[62:63]
	v_lshl_or_b32 v60, s39, 2, v1
	v_div_fmas_f32 v47, v47, v64, v66
	v_lshlrev_b64 v[66:67], 12, v[62:63]
	v_div_fixup_f32 v64, v47, v179, 1.0
	v_lshl_add_u64 v[66:67], s[86:87], 0, v[66:67]
	v_lshlrev_b32_e32 v68, 8, v60
	v_mov_b32_e32 v69, v46
	v_lshl_add_u64 v[66:67], v[66:67], 0, v[68:69]
	v_pk_mul_f32 v[70:71], v[152:153], v[64:65] op_sel_hi:[1,0]
	v_lshl_add_u64 v[66:67], v[176:177], 1, v[66:67]
	v_pk_mul_f32 v[68:69], v[154:155], v[64:65] op_sel_hi:[1,0]
	v_cvt_pk_bf16_f32 v70, v70, v71
	v_mov_b32_e32 v61, v46
	v_cvt_pk_bf16_f32 v71, v68, v69
	global_store_dwordx2 v[66:67], v[70:71], off
	v_pk_mul_f32 v[70:71], v[64:65], v[148:149] op_sel_hi:[0,1]
	v_pk_mul_f32 v[68:69], v[64:65], v[150:151] op_sel_hi:[0,1]
	v_cvt_pk_bf16_f32 v70, v70, v71
	v_cvt_pk_bf16_f32 v71, v68, v69
	global_store_dwordx2 v[66:67], v[70:71], off offset:32
	v_pk_mul_f32 v[70:71], v[64:65], v[144:145] op_sel_hi:[0,1]
	v_pk_mul_f32 v[68:69], v[64:65], v[146:147] op_sel_hi:[0,1]
	v_cvt_pk_bf16_f32 v70, v70, v71
	v_cvt_pk_bf16_f32 v71, v68, v69
	global_store_dwordx2 v[66:67], v[70:71], off offset:64
	v_pk_mul_f32 v[70:71], v[64:65], v[140:141] op_sel_hi:[0,1]
	v_pk_mul_f32 v[68:69], v[64:65], v[142:143] op_sel_hi:[0,1]
	v_cvt_pk_bf16_f32 v70, v70, v71
	v_cvt_pk_bf16_f32 v71, v68, v69
	global_store_dwordx2 v[66:67], v[70:71], off offset:96
	v_pk_mul_f32 v[70:71], v[64:65], v[132:133] op_sel_hi:[0,1]
	v_pk_mul_f32 v[68:69], v[64:65], v[134:135] op_sel_hi:[0,1]
	v_cvt_pk_bf16_f32 v70, v70, v71
	v_cvt_pk_bf16_f32 v71, v68, v69
	global_store_dwordx2 v[66:67], v[70:71], off offset:128
	v_pk_mul_f32 v[70:71], v[64:65], v[128:129] op_sel_hi:[0,1]
	v_pk_mul_f32 v[68:69], v[64:65], v[130:131] op_sel_hi:[0,1]
	v_cvt_pk_bf16_f32 v70, v70, v71
	v_cvt_pk_bf16_f32 v71, v68, v69
	global_store_dwordx2 v[66:67], v[70:71], off offset:160
	v_pk_mul_f32 v[68:69], v[64:65], v[126:127] op_sel_hi:[0,1]
	v_pk_mul_f32 v[70:71], v[64:65], v[124:125] op_sel_hi:[0,1]
	v_cvt_pk_bf16_f32 v70, v70, v71
	v_cvt_pk_bf16_f32 v71, v68, v69
	v_pk_mul_f32 v[68:69], v[64:65], v[138:139] op_sel_hi:[0,1]
	v_pk_mul_f32 v[64:65], v[64:65], v[136:137] op_sel_hi:[0,1]
	global_store_dwordx2 v[66:67], v[70:71], off offset:192
	v_cvt_pk_bf16_f32 v64, v64, v65
	v_cvt_pk_bf16_f32 v65, v68, v69
	global_store_dwordx2 v[66:67], v[64:65], off offset:224
	s_and_saveexec_b64 s[22:23], s[18:19]
	s_cbranch_execz .LBB0_456
	v_cmp_gt_f32_e32 vcc, s56, v179
	v_lshlrev_b64 v[62:63], 6, v[62:63]
	v_lshl_add_u64 v[62:63], s[72:73], 0, v[62:63]
	v_cndmask_b32_e64 v64, 0, 32, vcc
	v_ldexp_f32 v64, v179, v64
	v_log_f32_e32 v64, v64
	v_cndmask_b32_e32 v47, 0, v227, vcc
	v_lshl_add_u64 v[62:63], v[60:61], 2, v[62:63]
	v_sub_f32_e32 v47, v64, v47
	v_add_f32_e32 v47, v231, v47
	global_store_dword v[62:63], v47, off
